# baseline (speedup 1.0000x reference)
.Lmk_ua_ready:
	s_waitcnt lgkmcnt(8)
	v_mfma_f32_16x16x32_f16 v[200:203], v[240:243], v[208:211], 0
	v_mfma_f32_16x16x32_f16 v[160:163], v[240:243], v[216:219], 0
	v_mfma_f32_16x16x32_f16 v[248:251], v[240:243], v[224:227], 0
	v_mfma_f32_16x16x32_f16 v[252:255], v[240:243], v[232:235], 0
	v_mfma_f32_16x16x32_f16 v[200:203], v[244:247], v[212:215], v[200:203]
	v_mfma_f32_16x16x32_f16 v[160:163], v[244:247], v[220:223], v[160:163]
	v_mfma_f32_16x16x32_f16 v[248:251], v[244:247], v[228:231], v[248:251]
	v_mfma_f32_16x16x32_f16 v[252:255], v[244:247], v[236:239], v[252:255]
	ds_read_b64_tr_b16 v[146:147], v186 offset:4096
	ds_read_b64_tr_b16 v[148:149], v186 offset:6144
	ds_read_b64_tr_b16 v[150:151], v188 offset:4096
	ds_read_b64_tr_b16 v[152:153], v188 offset:6144
	ds_read_b64_tr_b16 v[154:155], v189 offset:4096
	ds_read_b64_tr_b16 v[156:157], v189 offset:6144
	ds_read_b64_tr_b16 v[204:205], v190 offset:4096
	ds_read_b64_tr_b16 v[206:207], v190 offset:6144
	v_add_u32_e32 v229, s82, v172
	ds_read2_b32 v[224:225], v229 offset1:8
	ds_read2_b32 v[226:227], v229 offset0:16 offset1:24
	ds_read2_b32 v[232:233], v229 offset0:32 offset1:40
	ds_read2_b32 v[234:235], v229 offset0:48 offset1:56
	v_cndmask_b32_e64 v34, v200, v160, s[60:61]
	v_cndmask_b32_e64 v34, v34, v248, s[62:63]
	v_cndmask_b32_e64 v34, v34, v252, s[64:65]
.Lmk_half_join:
	v_add_f32_e32 v34, v34, v121
	v_mul_f32_e32 v121, 0x3e4ccccd, v34
	v_max_f32_e32 v34, v34, v121
	v_cmp_gt_f32_e32 vcc, v34, v184
	s_and_b64 s[68:69], s[56:57], vcc
	s_cmp_eq_u64 s[68:69], 0
	s_cbranch_scc0 .Lmk_max
	v_add_u32_e32 v230, s82, v173
	v_bfe_u32 v121, v183, 16, 4
	ds_read_b32 v183, v230

.Lmk_max:
	v_cndmask_b32_e64 v161, v185, v34, s[56:57]
	s_nop 1
	v_max_f32_dpp v161, v161, v161 row_shr:1 row_mask:0xf bank_mask:0xf
	v_bfe_u32 v121, v183, 16, 4
	s_nop 0
	v_max_f32_dpp v161, v161, v161 row_shr:2 row_mask:0xf bank_mask:0xf
	s_nop 0
	v_add_u32_e32 v230, s82, v173
	v_max_f32_dpp v161, v161, v161 row_shr:4 row_mask:0xf bank_mask:0xf
	s_nop 1
	v_max_f32_dpp v161, v161, v161 row_shr:8 row_mask:0xf bank_mask:0xf
	s_nop 1
	v_max_f32_dpp v161, v161, v161 row_bcast:15 row_mask:0xa bank_mask:0xf
	s_nop 1
	v_max_f32_dpp v161, v161, v161 row_bcast:31 row_mask:0xc bank_mask:0xf
	s_nop 1
	v_readlane_b32 s70, v161, 63
	ds_read_b32 v183, v230
	s_and_b64 vcc, exec, s[54:55]
	s_nop 0
	v_mov_b32_e32 v161, s70
	s_cbranch_vccz .Lmk_rescale

.Lmk_half_iter:
	s_cmp_lt_i32 s66, 17
	s_cbranch_scc1 .Lmk_quarter_iter
	ds_read_b128 v[208:211], v122
	ds_read_b128 v[212:215], v117
	ds_read_b128 v[216:219], v122 offset:2048
	ds_read_b128 v[220:223], v117 offset:2048
	ds_read_b64_tr_b16 v[130:131], v186 offset:0
	ds_read_b64_tr_b16 v[132:133], v186 offset:2048
	ds_read_b64_tr_b16 v[134:135], v188 offset:0
	ds_read_b64_tr_b16 v[136:137], v188 offset:2048
	ds_read_b64_tr_b16 v[138:139], v189 offset:0
	ds_read_b64_tr_b16 v[140:141], v189 offset:2048
	ds_read_b64_tr_b16 v[142:143], v190 offset:0
	ds_read_b64_tr_b16 v[144:145], v190 offset:2048
	s_waitcnt lgkmcnt(8)
	v_mfma_f32_16x16x32_f16 v[200:203], v[240:243], v[208:211], 0
	v_mfma_f32_16x16x32_f16 v[160:163], v[240:243], v[216:219], 0
	v_mfma_f32_16x16x32_f16 v[200:203], v[244:247], v[212:215], v[200:203]
	v_mfma_f32_16x16x32_f16 v[160:163], v[244:247], v[220:223], v[160:163]
	v_add_u32_e32 v229, s82, v172
	ds_read2_b32 v[224:225], v229 offset1:8
	ds_read2_b32 v[226:227], v229 offset0:16 offset1:24
	ds_read2_b32 v[232:233], v229 offset0:32 offset1:40
	ds_read2_b32 v[234:235], v229 offset0:48 offset1:56
	s_nop 2
	v_cndmask_b32_e64 v34, v200, v160, s[60:61]
	s_branch .Lmk_half_join
.Lmk_quarter_iter:
	ds_read_b128 v[208:211], v122
	ds_read_b128 v[212:215], v117
	ds_read_b64_tr_b16 v[130:131], v186 offset:0
	ds_read_b64_tr_b16 v[134:135], v188 offset:0
	ds_read_b64_tr_b16 v[138:139], v189 offset:0
	ds_read_b64_tr_b16 v[142:143], v190 offset:0
	s_waitcnt lgkmcnt(4)
	v_mfma_f32_16x16x32_f16 v[200:203], v[240:243], v[208:211], 0
	v_mfma_f32_16x16x32_f16 v[200:203], v[244:247], v[212:215], v[200:203]
	v_add_u32_e32 v229, s82, v172
	ds_read2_b32 v[224:225], v229 offset1:8
	ds_read2_b32 v[226:227], v229 offset0:16 offset1:24
	ds_read2_b32 v[232:233], v229 offset0:32 offset1:40
	ds_read2_b32 v[234:235], v229 offset0:48 offset1:56
	s_nop 2
	v_mov_b32_e32 v34, v200
	s_branch .Lmk_half_join
